# passCU: priority graded by dispatch order (second block per CU above first, waves 4-7 above 0-3)
# baseline (speedup 1.0000x reference)
.LBB8_4:
	s_load_dwordx2 s[12:13], s[0:1], 0xa8
	s_load_dwordx2 s[18:19], s[0:1], 0x98
	s_waitcnt lgkmcnt(0)
	s_sub_i32 s4, s28, s20
	s_add_i32 s4, s4, 31
	v_and_b32_e32 v1, 63, v0
	s_ashr_i32 s15, s4, 5
	s_cmp_lt_i32 s15, 1
	v_add_u32_e32 v90, s14, v98
	v_and_b32_e32 v100, 32, v0
	v_lshlrev_b32_e32 v99, 4, v1
	s_cbranch_scc1 .LBB8_7
	s_load_dwordx8 s[4:11], s[0:1], 0x0
	s_load_dwordx2 s[24:25], s[0:1], 0x20
	s_load_dwordx2 s[30:31], s[0:1], 0x80
	s_load_dwordx2 s[48:49], s[0:1], 0x90
	v_and_b32_e32 v34, 7, v1
	v_lshlrev_b32_e32 v34, 4, v34
	v_lshrrev_b32_e32 v35, 3, v1
	s_lshl_b32 s32, s3, 12
	s_add_i32 s33, s32, 0x2000
	s_add_i32 s32, s32, 0xb500
	s_cmp_lt_u32 s3, 2
	s_cselect_b32 s32, s33, s32
	v_lshlrev_b32_e32 v36, 1, v35
	v_and_b32_e32 v36, 7, v36
	v_or_b32_e32 v37, 1, v36
	v_lshlrev_b32_e32 v36, 4, v36
	v_lshlrev_b32_e32 v37, 4, v37
	v_xor_b32_e32 v36, v36, v34
	v_xor_b32_e32 v37, v37, v34
	v_lshl_add_u32 v39, v35, 9, s32
	v_add_u32_e32 v36, v36, v39
	v_add_u32_e32 v37, v37, v39
	v_lshrrev_b32_e32 v38, 1, v98
	v_and_b32_e32 v38, 7, v38
	v_lshrrev_b32_e32 v39, 3, v100
	v_xor_b32_e32 v38, v38, v39
	v_lshlrev_b32_e32 v38, 4, v38
	v_lshl_add_u32 v39, v98, 7, s32
	v_add_u32_e32 v38, v38, v39
	v_lshlrev_b32_e32 v35, 4, v35
	s_mov_b32 s35, 0x1869f
	s_mov_b32 s65, 0xffff0000
	v_mov_b32_e32 v2, 0
	v_mov_b32_e32 v3, 0
	v_mov_b32_e32 v4, 0
	v_mov_b32_e32 v5, 0
	v_mov_b32_e32 v6, 0
	v_mov_b32_e32 v7, 0
	v_mov_b32_e32 v8, 0
	v_mov_b32_e32 v9, 0
	v_mov_b32_e32 v10, 0
	v_mov_b32_e32 v11, 0
	v_mov_b32_e32 v12, 0
	v_mov_b32_e32 v13, 0
	v_mov_b32_e32 v14, 0
	v_mov_b32_e32 v15, 0
	v_mov_b32_e32 v16, 0
	v_mov_b32_e32 v17, 0
	v_mov_b32_e32 v18, 0
	v_mov_b32_e32 v19, 0
	v_mov_b32_e32 v20, 0
	v_mov_b32_e32 v21, 0
	v_mov_b32_e32 v22, 0
	v_mov_b32_e32 v23, 0
	v_mov_b32_e32 v24, 0
	v_mov_b32_e32 v25, 0
	v_mov_b32_e32 v26, 0
	v_mov_b32_e32 v27, 0
	v_mov_b32_e32 v28, 0
	v_mov_b32_e32 v29, 0
	v_mov_b32_e32 v30, 0
	v_mov_b32_e32 v31, 0
	v_mov_b32_e32 v32, 0
	v_mov_b32_e32 v33, 0
	s_waitcnt vmcnt(0) lgkmcnt(0)
	v_mov_b32_e32 v42, v70
	v_mov_b32_e32 v43, v71
	v_mov_b32_e32 v44, v72
	v_mov_b32_e32 v45, v73
	v_mov_b32_e32 v46, v74
	v_mov_b32_e32 v47, v75
	v_mov_b32_e32 v48, v76
	v_mov_b32_e32 v49, v77
	v_mov_b32_e32 v50, v78
	v_mov_b32_e32 v51, v79
	v_mov_b32_e32 v52, v80
	v_mov_b32_e32 v53, v81
	v_lshlrev_b32_e32 v39, 2, v90
	global_load_dword v40, v39, s[30:31]
	global_load_dword v41, v39, s[30:31] offset:4
	s_lshl_b32 s34, s20, 2
	v_min_u32_e32 v42, s35, v42
	v_min_u32_e32 v46, s35, v46
	v_min_u32_e32 v43, s35, v43
	v_min_u32_e32 v47, s35, v47
	v_min_u32_e32 v44, s35, v44
	v_min_u32_e32 v48, s35, v48
	v_min_u32_e32 v45, s35, v45
	v_min_u32_e32 v49, s35, v49
	v_lshl_or_b32 v42, v42, 7, v34
	v_lshl_or_b32 v46, v46, 7, v34
	v_lshl_or_b32 v43, v43, 7, v34
	v_lshl_or_b32 v47, v47, 7, v34
	v_lshl_or_b32 v44, v44, 7, v34
	v_lshl_or_b32 v48, v48, 7, v34
	v_lshl_or_b32 v45, v45, 7, v34
	v_lshl_or_b32 v49, v49, 7, v34
	global_load_dwordx4 v[70:73], v42, s[24:25]
	global_load_dwordx4 v[74:77], v43, s[24:25]
	global_load_dwordx4 v[78:81], v44, s[24:25]
	global_load_dwordx4 v[82:85], v45, s[24:25]
	global_load_dwordx4 v[86:89], v46, s[10:11]
	global_load_dwordx4 v[90:93], v47, s[10:11]
	global_load_dwordx4 v[94:97], v48, s[10:11]
	global_load_dwordx4 v[102:105], v49, s[10:11]
	s_add_i32 s34, s34, 0x80
	v_add_u32_e32 v39, s34, v35
	global_load_dwordx4 v[42:45], v39, s[4:5]
	global_load_dwordx4 v[46:49], v39, s[6:7]
	s_bitcmp1_b32 s2, 8
	s_cbranch_scc0 .Lcu_nopri2
	s_setprio 2
.Lcu_nopri2:
	s_cmp_lt_u32 s3, 4
	s_cbranch_scc1 .Lcu_nopri
	s_bitcmp1_b32 s2, 8
	s_cbranch_scc1 .Lcu_pr3
	s_setprio 1
	s_branch .Lcu_nopri
.Lcu_pr3:
	s_setprio 3
